# P3 GLA scan: state update split between wave 0 (row tiles 0-3) and wave 7 (row tiles 4-7)
# baseline (speedup 1.0000x reference)
; #define LAS __attribute__((address_space(3)))
; __device__ __forceinline__ unsigned f2bf(float f) { unsigned u = __builtin_bit_cast(unsigned, f); return (u + 0x7fffu + ((u >> 16) & 1u)) >> 16; }
; __device__ __forceinline__ void gla_scan_chain(Frame& F, int chain) {
;     ...
;         } else if (wave <= 4) {
;             const int m = wave - 1, r = 16 * m + fr;
;             bf16x8 vf[2]; gs_vfrag(base + GS_V, lane, vf);
;             const LAS unsigned char* sb = F.lds + GS_SB + (n & 1) * GS_SBBUF + fr * GS_SBROW + 16 * fq;
;             bf16x8 af[2], qf[4], sf[4];
; #pragma unroll
;             for (int ks = 0; ks < 2; ++ks) af[ks] = *(const LAS bf16x8*)(base + GS_AM + r * 128 + (((4 * ks + fq) ^ (r & 7)) * 16));
; #pragma unroll
;             for (int ks = 0; ks < 4; ++ks) { qf[ks] = *(const LAS bf16x8*)(base + GS_QIN + r * 256 + (((4 * ks + fq) ^ (r & 15)) * 16)); sf[ks] = *(const LAS bf16x8*)(sb + 64 * ks); }
;             __builtin_amdgcn_sched_barrier(0);
;             f32x4 acc = (f32x4){0.f, 0.f, 0.f, 0.f};
; #pragma unroll
;             for (int ks = 0; ks < 2; ++ks) acc = __builtin_amdgcn_mfma_f32_16x16x32_bf16(af[ks], vf[ks], acc, 0, 0, 0);
; #pragma unroll
;             for (int ks = 0; ks < 4; ++ks) acc = __builtin_amdgcn_mfma_f32_16x16x32_bf16(qf[ks], sf[ks], acc, 0, 0, 0);
;             bf16_t* op = ORAW + ((size_t)b * SEQ + 64 * n + 16 * m + 4 * fq) * 2048 + h * 256 + et * 16 + fr;
; #pragma unroll
;             for (int i = 0; i < 4; ++i) op[(size_t)i * 2048] = (bf16_t)f2bf(acc[i]);
;         }
.LBB0_375:
	s_andn2_b64 vcc, exec, s[10:11]
	s_cbranch_vccnz .Lgs_w567
	v_add_u32_e32 v3, s34, v92
	v_add3_u32 v3, v3, v93, s51
	ds_read_b64_tr_b16 v[112:113], v3
	ds_read_b64_tr_b16 v[114:115], v3 offset:128
	ds_read_b64_tr_b16 v[108:109], v3 offset:1024
	ds_read_b64_tr_b16 v[110:111], v3 offset:1152
	s_waitcnt lgkmcnt(0)
	v_add_u32_e32 v3, s34, v95
	v_add_u32_e32 v4, v3, v98
	s_bitcmp1_b32 s37, 0
	v_add_u32_e32 v3, v3, v99
	ds_read_b128 v[116:119], v4
	ds_read_b128 v[120:123], v3
	v_add_u32_e32 v4, s34, v96
	s_cselect_b32 s30, 0x1100, 0
	v_add_u32_e32 v5, v4, v100
	v_add_u32_e32 v3, s30, v104
	v_add_u32_e32 v128, v4, v101
	ds_read_b128 v[124:127], v5 offset:8192
	ds_read_b128 v[132:135], v128 offset:8192
	ds_read_b128 v[136:139], v3
	ds_read_b128 v[140:143], v3 offset:64
	v_add_u32_e32 v5, v4, v102
	v_add_u32_e32 v4, v4, v103
	ds_read_b128 v[144:147], v5 offset:8192
	ds_read_b128 v[148:151], v4 offset:8192
	ds_read_b128 v[156:159], v3 offset:128
	ds_read_b128 v[160:163], v3 offset:192
	s_waitcnt lgkmcnt(0)
	v_mfma_f32_16x16x32_bf16 v[112:115], v[116:119], v[112:115], 0
	v_lshl_add_u64 v[4:5], v[90:91], 0, s[18:19]
	s_mov_b32 s30, 0x61ff1000
	v_mfma_f32_16x16x32_bf16 v[108:111], v[120:123], v[108:111], v[112:115]
	v_mfma_f32_16x16x32_bf16 v[108:111], v[124:127], v[136:139], v[108:111]
	s_nop 3
	v_add_co_u32_e32 v112, vcc, s30, v4
	v_mfma_f32_16x16x32_bf16 v[108:111], v[132:135], v[140:143], v[108:111]
	s_nop 0
	v_addc_co_u32_e32 v113, vcc, 0, v5, vcc
	v_add_co_u32_e32 v114, vcc, 0x61ff2000, v4
	v_mfma_f32_16x16x32_bf16 v[108:111], v[144:147], v[156:159], v[108:111]
	s_nop 0
	v_addc_co_u32_e32 v115, vcc, 0, v5, vcc
	v_add_co_u32_e32 v4, vcc, 0x61ff3000, v4
	v_mfma_f32_16x16x32_bf16 v[108:111], v[148:151], v[160:163], v[108:111]
	s_nop 0
	v_addc_co_u32_e32 v5, vcc, 0, v5, vcc
	s_nop 5
	v_bfe_u32 v3, v108, 16, 1
	v_bfe_u32 v116, v109, 16, 1
	v_bfe_u32 v117, v110, 16, 1
	v_bfe_u32 v118, v111, 16, 1
	v_add3_u32 v3, v108, v3, s65
	v_add3_u32 v108, v109, v116, s65
	v_add3_u32 v109, v110, v117, s65
	global_store_short_d16_hi v[112:113], v3, off offset:-4096
	global_store_short_d16_hi v[112:113], v108, off
	global_store_short_d16_hi v[114:115], v109, off
	v_add3_u32 v3, v111, v118, s65
	global_store_short_d16_hi v[4:5], v3, off
	s_branch .LBB0_377
.Lgs_w567:
	s_and_b64 vcc, exec, s[16:17]
	s_cbranch_vccnz .LBB0_378

; #define LAS __attribute__((address_space(3)))
; __device__ __forceinline__ unsigned cvtpk(float lo, float hi) { f32x2 v = {lo, hi}; bf16x2_t b = __builtin_convertvector(v, bf16x2_t); return __builtin_bit_cast(unsigned, b); }
; __device__ __forceinline__ void gla_scan_chain(Frame& F, int chain) {
;     ...
;         if (wave == 0) {
;             bf16x8 vf[2]; gs_vfrag(base + GS_V, lane, vf);
;             bf16x8 kf[8][2]; f32x4 dc[8];
; #pragma unroll
;             for (int mt = 0; mt < 8; ++mt) { const int r = 16 * mt + fr; dc[mt] = *(const LAS f32x4*)(base + GS_DEC + (16 * mt + 4 * fq) * 4);
; #pragma unroll
;                 for (int ks = 0; ks < 2; ++ks) kf[mt][ks] = *(const LAS bf16x8*)(base + GS_KDT + r * 128 + (((4 * ks + fq) ^ (r & 7)) * 16)); }
;             __builtin_amdgcn_sched_barrier(0);
;             LAS unsigned char* sb = F.lds + GS_SB + ((n + 1) & 1) * GS_SBBUF + fr * GS_SBROW + 8 * fq;
; #pragma unroll
;             for (int mt = 0; mt < 8; ++mt) { f32x4 s = S[mt] * dc[mt];
;                 s = __builtin_amdgcn_mfma_f32_16x16x32_bf16(kf[mt][0], vf[0], s, 0, 0, 0); s = __builtin_amdgcn_mfma_f32_16x16x32_bf16(kf[mt][1], vf[1], s, 0, 0, 0); S[mt] = s; }
; #pragma unroll
;             for (int mt = 0; mt < 8; ++mt) { u32x2 w; w.x = cvtpk(S[mt][0], S[mt][1]); w.y = cvtpk(S[mt][2], S[mt][3]); *(LAS u32x2*)(sb + 32 * mt) = w; }
.LBB0_378:
	v_readlane_b32 s30, v254, 23
	v_add_u32_e32 v3, s34, v92
	v_add3_u32 v3, v3, v93, s51
	ds_read_b64_tr_b16 v[112:113], v3
	ds_read_b64_tr_b16 v[114:115], v3 offset:128
	ds_read_b64_tr_b16 v[108:109], v3 offset:1024
	ds_read_b64_tr_b16 v[110:111], v3 offset:1152
	s_lshr_b32 s31, s30, 2
	s_lshl_b32 s30, s31, 8
	v_add_u32_e32 v3, s34, v94
	v_add_u32_e32 v3, s30, v3
	s_lshl_b32 s30, s31, 13
	v_add_u32_e32 v4, s34, v97
	v_add_u32_e32 v4, s30, v4
	v_add_u32_e32 v5, v4, v98
	v_add_u32_e32 v4, v4, v99
	ds_read_b128 v[116:119], v3 offset:43008
	ds_read_b128 v[120:123], v3 offset:43072
	ds_read_b128 v[124:127], v5 offset:24576
	ds_read_b128 v[132:135], v5 offset:26624
	ds_read_b128 v[136:139], v4 offset:24576
	ds_read_b128 v[140:143], v4 offset:26624
	ds_read_b128 v[144:147], v3 offset:43136
	ds_read_b128 v[148:151], v3 offset:43200
	ds_read_b128 v[156:159], v5 offset:28672
	ds_read_b128 v[160:163], v5 offset:30720
	ds_read_b128 v[164:167], v4 offset:28672
	ds_read_b128 v[170:173], v4 offset:30720
	s_andn2_b32 s30, 1, s37
	s_mulk_i32 s30, 0x1100
	s_lshl_b32 s31, s31, 7
	s_add_i32 s30, s30, s31
	s_waitcnt lgkmcnt(6)
	v_pk_mul_f32 v[12:13], v[12:13], v[118:119]
	v_pk_mul_f32 v[10:11], v[10:11], v[116:117]
	v_pk_mul_f32 v[16:17], v[16:17], v[122:123]
	v_pk_mul_f32 v[14:15], v[14:15], v[120:121]
	v_add_u32_e32 v3, s30, v105
	s_nop 0
	v_mfma_f32_16x16x32_bf16 v[10:13], v[124:127], v[112:115], v[10:13]
	v_mfma_f32_16x16x32_bf16 v[14:17], v[132:135], v[112:115], v[14:17]
	s_waitcnt lgkmcnt(0)
	v_pk_mul_f32 v[18:19], v[18:19], v[144:145]
	v_pk_mul_f32 v[20:21], v[20:21], v[146:147]
	v_pk_mul_f32 v[22:23], v[22:23], v[148:149]
	v_pk_mul_f32 v[24:25], v[24:25], v[150:151]
	v_mfma_f32_16x16x32_bf16 v[10:13], v[136:139], v[108:111], v[10:13]
	v_mfma_f32_16x16x32_bf16 v[14:17], v[140:143], v[108:111], v[14:17]
	v_mfma_f32_16x16x32_bf16 v[18:21], v[156:159], v[112:115], v[18:21]
	v_mfma_f32_16x16x32_bf16 v[22:25], v[160:163], v[112:115], v[22:25]
	v_mfma_f32_16x16x32_bf16 v[18:21], v[164:167], v[108:111], v[18:21]
	v_mfma_f32_16x16x32_bf16 v[22:25], v[170:173], v[108:111], v[22:25]
	s_nop 3
	v_cvt_pk_bf16_f32 v4, v10, v11
	v_cvt_pk_bf16_f32 v5, v12, v13
	v_cvt_pk_bf16_f32 v116, v14, v15
	v_cvt_pk_bf16_f32 v117, v16, v17
	ds_write2_b64 v3, v[4:5], v[116:117] offset1:4
	s_nop 7
	v_cvt_pk_bf16_f32 v4, v18, v19
	v_cvt_pk_bf16_f32 v5, v20, v21
	v_cvt_pk_bf16_f32 v116, v22, v23
	v_cvt_pk_bf16_f32 v117, v24, v25
	ds_write2_b64 v3, v[4:5], v[116:117] offset0:8 offset1:12
	s_and_b64 vcc, exec, s[4:5]
	s_cbranch_vccnz .LBB0_360
